# h0 reads the modulation vectors with coherent (sc1) loads (they are stored write-through) instead of a CU-wide invalidate after the counter wait
# baseline (speedup 1.0000x reference)
.LBB0_72:
	s_or_b64 exec, exec, s[0:1]
	s_waitcnt lgkmcnt(0)
	s_mov_b32 s0, s98
	v_mbcnt_lo_u32_b32 v0, -1, 0
	v_mbcnt_hi_u32_b32 v0, -1, v0
	s_nop 1
	v_lshl_add_u32 v0, s0, 6, v0
	s_nop 0
	v_cmp_eq_u32_e32 vcc, 0, v0
	s_and_saveexec_b64 s[0:1], vcc
	s_cbranch_execz .LBB0_74
	s_waitcnt vmcnt(0)
	s_waitcnt vmcnt(0)

.LBB0_77:
	v_add_u32_e32 v93, s3, v92
	v_add_u32_e32 v90, s21, v92
	v_add_u32_e32 v88, s22, v92
	s_add_u32 s18, s78, 0x8500000
	s_addc_u32 s19, s79, 0
	s_add_u32 s4, s96, 0x1000
	s_addc_u32 s5, s97, 0
	v_lshl_add_u32 v94, v92, 12, v64
	v_ashrrev_i32_e32 v106, 13, v92
	v_mul_i32_i24_e32 v106, 0x6000, v106
	v_add_u32_e32 v98, v106, v64
	global_load_dwordx4 v[0:3], v94, s[48:49] nt
	global_load_dwordx4 v[4:7], v94, s[48:49] offset:1024 nt
	global_load_dwordx4 v[8:11], v94, s[48:49] offset:2048 nt
	global_load_dwordx4 v[12:15], v94, s[48:49] offset:3072 nt
	global_load_dwordx4 v[112:115], v98, s[96:97] sc1
	global_load_dwordx4 v[120:123], v98, s[96:97] offset:1024 sc1
	global_load_dwordx4 v[128:131], v98, s[96:97] offset:2048 sc1
	global_load_dwordx4 v[136:139], v98, s[96:97] offset:3072 sc1
	global_load_dwordx4 v[116:119], v98, s[4:5] sc1
	global_load_dwordx4 v[124:127], v98, s[4:5] offset:1024 sc1
	global_load_dwordx4 v[132:135], v98, s[4:5] offset:2048 sc1
	global_load_dwordx4 v[140:143], v98, s[4:5] offset:3072 sc1
	v_lshl_add_u32 v102, v92, 11, v70
	v_cmp_gt_i32_e32 vcc, s20, v93
	s_and_saveexec_b64 s[0:1], vcc
	v_lshl_add_u32 v95, v93, 12, v64
	v_ashrrev_i32_e32 v106, 13, v93
	v_mul_i32_i24_e32 v106, 0x6000, v106
	v_add_u32_e32 v99, v106, v64
	global_load_dwordx4 v[16:19], v95, s[48:49] nt
	global_load_dwordx4 v[20:23], v95, s[48:49] offset:1024 nt
	global_load_dwordx4 v[24:27], v95, s[48:49] offset:2048 nt
	global_load_dwordx4 v[28:31], v95, s[48:49] offset:3072 nt
	global_load_dwordx4 v[144:147], v99, s[96:97] sc1
	global_load_dwordx4 v[152:155], v99, s[96:97] offset:1024 sc1
	global_load_dwordx4 v[160:163], v99, s[96:97] offset:2048 sc1
	global_load_dwordx4 v[168:171], v99, s[96:97] offset:3072 sc1
	global_load_dwordx4 v[148:151], v99, s[4:5] sc1
	global_load_dwordx4 v[156:159], v99, s[4:5] offset:1024 sc1
	global_load_dwordx4 v[164:167], v99, s[4:5] offset:2048 sc1
	global_load_dwordx4 v[172:175], v99, s[4:5] offset:3072 sc1
	v_lshl_add_u32 v103, v93, 11, v70
	s_or_b64 exec, exec, s[0:1]
	v_cmp_gt_i32_e32 vcc, s20, v90
	s_and_saveexec_b64 s[0:1], vcc
	v_lshl_add_u32 v96, v90, 12, v64
	v_ashrrev_i32_e32 v106, 13, v90
	v_mul_i32_i24_e32 v106, 0x6000, v106
	v_add_u32_e32 v100, v106, v64
	global_load_dwordx4 v[32:35], v96, s[48:49] nt
	global_load_dwordx4 v[36:39], v96, s[48:49] offset:1024 nt
	global_load_dwordx4 v[40:43], v96, s[48:49] offset:2048 nt
	global_load_dwordx4 v[44:47], v96, s[48:49] offset:3072 nt
	global_load_dwordx4 v[176:179], v100, s[96:97] sc1
	global_load_dwordx4 v[184:187], v100, s[96:97] offset:1024 sc1
	global_load_dwordx4 v[192:195], v100, s[96:97] offset:2048 sc1
	global_load_dwordx4 v[200:203], v100, s[96:97] offset:3072 sc1
	global_load_dwordx4 v[180:183], v100, s[4:5] sc1
	global_load_dwordx4 v[188:191], v100, s[4:5] offset:1024 sc1
	global_load_dwordx4 v[196:199], v100, s[4:5] offset:2048 sc1
	global_load_dwordx4 v[204:207], v100, s[4:5] offset:3072 sc1
	v_lshl_add_u32 v104, v90, 11, v70
	s_or_b64 exec, exec, s[0:1]
	v_cmp_gt_i32_e32 vcc, s20, v88
	s_and_saveexec_b64 s[0:1], vcc
	v_lshl_add_u32 v97, v88, 12, v64
	v_ashrrev_i32_e32 v106, 13, v88
	v_mul_i32_i24_e32 v106, 0x6000, v106
	v_add_u32_e32 v101, v106, v64
	global_load_dwordx4 v[48:51], v97, s[48:49] nt
	global_load_dwordx4 v[52:55], v97, s[48:49] offset:1024 nt
	global_load_dwordx4 v[56:59], v97, s[48:49] offset:2048 nt
	global_load_dwordx4 v[60:63], v97, s[48:49] offset:3072 nt
	global_load_dwordx4 v[208:211], v101, s[96:97] sc1
	global_load_dwordx4 v[216:219], v101, s[96:97] offset:1024 sc1
	global_load_dwordx4 v[224:227], v101, s[96:97] offset:2048 sc1
	global_load_dwordx4 v[232:235], v101, s[96:97] offset:3072 sc1
	global_load_dwordx4 v[212:215], v101, s[4:5] sc1
	global_load_dwordx4 v[220:223], v101, s[4:5] offset:1024 sc1
	global_load_dwordx4 v[228:231], v101, s[4:5] offset:2048 sc1
	global_load_dwordx4 v[236:239], v101, s[4:5] offset:3072 sc1
	v_lshl_add_u32 v105, v88, 11, v70
	s_or_b64 exec, exec, s[0:1]
	s_waitcnt vmcnt(0)
	v_pk_add_f32 v[118:119], v[118:119], 1.0 op_sel_hi:[1,0]
	v_pk_add_f32 v[116:117], v[116:117], 1.0 op_sel_hi:[1,0]
	v_pk_add_f32 v[126:127], v[126:127], 1.0 op_sel_hi:[1,0]
	v_pk_add_f32 v[124:125], v[124:125], 1.0 op_sel_hi:[1,0]
	v_pk_add_f32 v[134:135], v[134:135], 1.0 op_sel_hi:[1,0]
	v_pk_add_f32 v[132:133], v[132:133], 1.0 op_sel_hi:[1,0]
	v_pk_add_f32 v[142:143], v[142:143], 1.0 op_sel_hi:[1,0]
	v_pk_add_f32 v[140:141], v[140:141], 1.0 op_sel_hi:[1,0]
	v_pk_fma_f32 v[2:3], v[2:3], v[118:119], v[114:115]
	v_pk_fma_f32 v[0:1], v[0:1], v[116:117], v[112:113]
	v_pk_fma_f32 v[6:7], v[6:7], v[126:127], v[122:123]
	v_pk_fma_f32 v[4:5], v[4:5], v[124:125], v[120:121]
	v_pk_fma_f32 v[10:11], v[10:11], v[134:135], v[130:131]
	v_pk_fma_f32 v[8:9], v[8:9], v[132:133], v[128:129]
	v_pk_fma_f32 v[14:15], v[14:15], v[142:143], v[138:139]
	v_pk_fma_f32 v[12:13], v[12:13], v[140:141], v[136:137]
	v_cvt_pk_bf16_f32 v0, v0, v1
	v_cvt_pk_bf16_f32 v1, v2, v3
	v_cvt_pk_bf16_f32 v4, v4, v5
	v_cvt_pk_bf16_f32 v5, v6, v7
	v_cvt_pk_bf16_f32 v8, v8, v9
	v_cvt_pk_bf16_f32 v9, v10, v11
	v_cvt_pk_bf16_f32 v12, v12, v13
	v_cvt_pk_bf16_f32 v13, v14, v15
	global_store_dwordx2 v102, v[0:1], s[18:19]
	global_store_dwordx2 v102, v[4:5], s[18:19] offset:512
	global_store_dwordx2 v102, v[8:9], s[18:19] offset:1024
	global_store_dwordx2 v102, v[12:13], s[18:19] offset:1536
	v_cmp_gt_i32_e32 vcc, s20, v93
	s_and_saveexec_b64 s[0:1], vcc
	v_pk_add_f32 v[150:151], v[150:151], 1.0 op_sel_hi:[1,0]
	v_pk_add_f32 v[148:149], v[148:149], 1.0 op_sel_hi:[1,0]
	v_pk_add_f32 v[158:159], v[158:159], 1.0 op_sel_hi:[1,0]
	v_pk_add_f32 v[156:157], v[156:157], 1.0 op_sel_hi:[1,0]
	v_pk_add_f32 v[166:167], v[166:167], 1.0 op_sel_hi:[1,0]
	v_pk_add_f32 v[164:165], v[164:165], 1.0 op_sel_hi:[1,0]
	v_pk_add_f32 v[174:175], v[174:175], 1.0 op_sel_hi:[1,0]
	v_pk_add_f32 v[172:173], v[172:173], 1.0 op_sel_hi:[1,0]
	v_pk_fma_f32 v[18:19], v[18:19], v[150:151], v[146:147]
	v_pk_fma_f32 v[16:17], v[16:17], v[148:149], v[144:145]
	v_pk_fma_f32 v[22:23], v[22:23], v[158:159], v[154:155]
	v_pk_fma_f32 v[20:21], v[20:21], v[156:157], v[152:153]
	v_pk_fma_f32 v[26:27], v[26:27], v[166:167], v[162:163]
	v_pk_fma_f32 v[24:25], v[24:25], v[164:165], v[160:161]
	v_pk_fma_f32 v[30:31], v[30:31], v[174:175], v[170:171]
	v_pk_fma_f32 v[28:29], v[28:29], v[172:173], v[168:169]
	v_cvt_pk_bf16_f32 v16, v16, v17
	v_cvt_pk_bf16_f32 v17, v18, v19
	v_cvt_pk_bf16_f32 v20, v20, v21
	v_cvt_pk_bf16_f32 v21, v22, v23
	v_cvt_pk_bf16_f32 v24, v24, v25
	v_cvt_pk_bf16_f32 v25, v26, v27
	v_cvt_pk_bf16_f32 v28, v28, v29
	v_cvt_pk_bf16_f32 v29, v30, v31
	global_store_dwordx2 v103, v[16:17], s[18:19]
	global_store_dwordx2 v103, v[20:21], s[18:19] offset:512
	global_store_dwordx2 v103, v[24:25], s[18:19] offset:1024
	global_store_dwordx2 v103, v[28:29], s[18:19] offset:1536
	s_or_b64 exec, exec, s[0:1]
	v_cmp_gt_i32_e32 vcc, s20, v90
	s_and_saveexec_b64 s[0:1], vcc
	v_pk_add_f32 v[182:183], v[182:183], 1.0 op_sel_hi:[1,0]
	v_pk_add_f32 v[180:181], v[180:181], 1.0 op_sel_hi:[1,0]
	v_pk_add_f32 v[190:191], v[190:191], 1.0 op_sel_hi:[1,0]
	v_pk_add_f32 v[188:189], v[188:189], 1.0 op_sel_hi:[1,0]
	v_pk_add_f32 v[198:199], v[198:199], 1.0 op_sel_hi:[1,0]
	v_pk_add_f32 v[196:197], v[196:197], 1.0 op_sel_hi:[1,0]
	v_pk_add_f32 v[206:207], v[206:207], 1.0 op_sel_hi:[1,0]
	v_pk_add_f32 v[204:205], v[204:205], 1.0 op_sel_hi:[1,0]
	v_pk_fma_f32 v[34:35], v[34:35], v[182:183], v[178:179]
	v_pk_fma_f32 v[32:33], v[32:33], v[180:181], v[176:177]
	v_pk_fma_f32 v[38:39], v[38:39], v[190:191], v[186:187]
	v_pk_fma_f32 v[36:37], v[36:37], v[188:189], v[184:185]
	v_pk_fma_f32 v[42:43], v[42:43], v[198:199], v[194:195]
	v_pk_fma_f32 v[40:41], v[40:41], v[196:197], v[192:193]
	v_pk_fma_f32 v[46:47], v[46:47], v[206:207], v[202:203]
	v_pk_fma_f32 v[44:45], v[44:45], v[204:205], v[200:201]
	v_cvt_pk_bf16_f32 v32, v32, v33
	v_cvt_pk_bf16_f32 v33, v34, v35
	v_cvt_pk_bf16_f32 v36, v36, v37
	v_cvt_pk_bf16_f32 v37, v38, v39
	v_cvt_pk_bf16_f32 v40, v40, v41
	v_cvt_pk_bf16_f32 v41, v42, v43
	v_cvt_pk_bf16_f32 v44, v44, v45
	v_cvt_pk_bf16_f32 v45, v46, v47
	global_store_dwordx2 v104, v[32:33], s[18:19]
	global_store_dwordx2 v104, v[36:37], s[18:19] offset:512
	global_store_dwordx2 v104, v[40:41], s[18:19] offset:1024
	global_store_dwordx2 v104, v[44:45], s[18:19] offset:1536
	s_or_b64 exec, exec, s[0:1]
	v_cmp_gt_i32_e32 vcc, s20, v88
	s_and_saveexec_b64 s[0:1], vcc
	v_pk_add_f32 v[214:215], v[214:215], 1.0 op_sel_hi:[1,0]
	v_pk_add_f32 v[212:213], v[212:213], 1.0 op_sel_hi:[1,0]
	v_pk_add_f32 v[222:223], v[222:223], 1.0 op_sel_hi:[1,0]
	v_pk_add_f32 v[220:221], v[220:221], 1.0 op_sel_hi:[1,0]
	v_pk_add_f32 v[230:231], v[230:231], 1.0 op_sel_hi:[1,0]
	v_pk_add_f32 v[228:229], v[228:229], 1.0 op_sel_hi:[1,0]
	v_pk_add_f32 v[238:239], v[238:239], 1.0 op_sel_hi:[1,0]
	v_pk_add_f32 v[236:237], v[236:237], 1.0 op_sel_hi:[1,0]
	v_pk_fma_f32 v[50:51], v[50:51], v[214:215], v[210:211]
	v_pk_fma_f32 v[48:49], v[48:49], v[212:213], v[208:209]
	v_pk_fma_f32 v[54:55], v[54:55], v[222:223], v[218:219]
	v_pk_fma_f32 v[52:53], v[52:53], v[220:221], v[216:217]
	v_pk_fma_f32 v[58:59], v[58:59], v[230:231], v[226:227]
	v_pk_fma_f32 v[56:57], v[56:57], v[228:229], v[224:225]
	v_pk_fma_f32 v[62:63], v[62:63], v[238:239], v[234:235]
	v_pk_fma_f32 v[60:61], v[60:61], v[236:237], v[232:233]
	v_cvt_pk_bf16_f32 v48, v48, v49
	v_cvt_pk_bf16_f32 v49, v50, v51
	v_cvt_pk_bf16_f32 v52, v52, v53
	v_cvt_pk_bf16_f32 v53, v54, v55
	v_cvt_pk_bf16_f32 v56, v56, v57
	v_cvt_pk_bf16_f32 v57, v58, v59
	v_cvt_pk_bf16_f32 v60, v60, v61
	v_cvt_pk_bf16_f32 v61, v62, v63
	global_store_dwordx2 v105, v[48:49], s[18:19]
	global_store_dwordx2 v105, v[52:53], s[18:19] offset:512
	global_store_dwordx2 v105, v[56:57], s[18:19] offset:1024
	global_store_dwordx2 v105, v[60:61], s[18:19] offset:1536
	s_or_b64 exec, exec, s[0:1]
	s_mov_b64 s[0:1], 0
	s_branch .LBB0_76
